# layer1 also uses a 4-deep load ring (with in-loop scale loads)
# speedup vs baseline: 1.0249x; 1.0090x over previous
.Lg1_sel_done:
	s_min_i32 s40, s41, 32
	s_add_i32 s40, s40, 3
	s_and_b32 s40, s40, 0x3c
	s_max_i32 s40, s40, 4
	v_mov_b32_e32 v2, 0
	v_mov_b32_e32 v3, 0
	v_mov_b32_e32 v4, 0
	v_mov_b32_e32 v5, 0
	v_mov_b32_e32 v6, 0
	v_mov_b32_e32 v7, 0
	v_mov_b32_e32 v8, 0
	v_mov_b32_e32 v9, 0
	v_mov_b32_e32 v10, 0
	v_mov_b32_e32 v11, 0
	v_mov_b32_e32 v12, 0
	v_mov_b32_e32 v13, 0
	v_mov_b32_e32 v14, 0
	v_mov_b32_e32 v15, 0
	v_mov_b32_e32 v16, 0
	v_mov_b32_e32 v17, 0
	v_mov_b32_e32 v18, 0
	s_waitcnt lgkmcnt(0)
	ds_bpermute_b32 v94, v90, v73 offset:0
	ds_bpermute_b32 v95, v90, v73 offset:4
	ds_bpermute_b32 v79, v90, v73 offset:8
	s_waitcnt lgkmcnt(1)
	v_and_b32_e32 v84, 0xffff, v94
	v_lshl_or_b32 v83, v84, 7, v89
	v_cmp_lt_i32_e32 vcc, 0, v78
	s_mov_b64 exec, vcc
	global_load_dwordx4 v[20:23], v83, s[12:13]
	s_mov_b64 exec, -1
	v_lshlrev_b32_e32 v109, 1, v84
	global_load_ushort v52, v109, s[14:15]
	v_lshrrev_b32_e32 v84, 16, v94
	v_lshl_or_b32 v83, v84, 7, v89
	v_cmp_lt_i32_e32 vcc, 1, v78
	s_mov_b64 exec, vcc
	global_load_dwordx4 v[24:27], v83, s[12:13]
	s_mov_b64 exec, -1
	v_lshlrev_b32_e32 v109, 1, v84
	global_load_ushort v53, v109, s[14:15]
	v_and_b32_e32 v84, 0xffff, v95
	v_lshl_or_b32 v83, v84, 7, v89
	v_cmp_lt_i32_e32 vcc, 2, v78
	s_mov_b64 exec, vcc
	global_load_dwordx4 v[28:31], v83, s[12:13]
	s_mov_b64 exec, -1
	v_lshlrev_b32_e32 v109, 1, v84
	global_load_ushort v54, v109, s[14:15]
	v_lshrrev_b32_e32 v84, 16, v95
	v_lshl_or_b32 v83, v84, 7, v89
	v_cmp_lt_i32_e32 vcc, 3, v78
	s_mov_b64 exec, vcc
	global_load_dwordx4 v[32:35], v83, s[12:13]
	s_mov_b64 exec, -1
	v_lshlrev_b32_e32 v109, 1, v84
	global_load_ushort v55, v109, s[14:15]
	s_cmp_le_u32 s40, 4
	s_cbranch_scc1 .Lg1_tail0
	s_waitcnt lgkmcnt(0)
	ds_bpermute_b32 v80, v90, v73 offset:12
	s_waitcnt vmcnt(6)
	v_cvt_f32_f16_e32 v52, v52
	v_cvt_f32_ubyte0_e32 v85, v20
	v_cvt_f32_ubyte1_e32 v86, v20
	v_cvt_f32_ubyte2_e32 v87, v20
	v_cvt_f32_ubyte3_e32 v88, v20
	v_fmac_f32_e32 v2, v85, v52
	v_fmac_f32_e32 v3, v86, v52
	v_fmac_f32_e32 v4, v87, v52
	v_fmac_f32_e32 v5, v88, v52
	v_cvt_f32_ubyte0_e32 v85, v21
	v_cvt_f32_ubyte1_e32 v86, v21
	v_cvt_f32_ubyte2_e32 v87, v21
	v_cvt_f32_ubyte3_e32 v88, v21
	v_fmac_f32_e32 v6, v85, v52
	v_fmac_f32_e32 v7, v86, v52
	v_fmac_f32_e32 v8, v87, v52
	v_fmac_f32_e32 v9, v88, v52
	v_cvt_f32_ubyte0_e32 v85, v22
	v_cvt_f32_ubyte1_e32 v86, v22
	v_cvt_f32_ubyte2_e32 v87, v22
	v_cvt_f32_ubyte3_e32 v88, v22
	v_fmac_f32_e32 v10, v85, v52
	v_fmac_f32_e32 v11, v86, v52
	v_fmac_f32_e32 v12, v87, v52
	v_fmac_f32_e32 v13, v88, v52
	v_cvt_f32_ubyte0_e32 v85, v23
	v_cvt_f32_ubyte1_e32 v86, v23
	v_cvt_f32_ubyte2_e32 v87, v23
	v_cvt_f32_ubyte3_e32 v88, v23
	v_fmac_f32_e32 v14, v85, v52
	v_fmac_f32_e32 v15, v86, v52
	v_fmac_f32_e32 v16, v87, v52
	v_fmac_f32_e32 v17, v88, v52
	v_add_f32_e32 v18, v18, v52
	v_and_b32_e32 v84, 0xffff, v79
	v_lshl_or_b32 v83, v84, 7, v89
	v_cmp_lt_i32_e32 vcc, 4, v78
	s_mov_b64 exec, vcc
	global_load_dwordx4 v[20:23], v83, s[12:13]
	s_mov_b64 exec, -1
	v_lshlrev_b32_e32 v109, 1, v84
	global_load_ushort v52, v109, s[14:15]
	s_waitcnt vmcnt(6)
	v_cvt_f32_f16_e32 v53, v53
	v_cvt_f32_ubyte0_e32 v85, v24
	v_cvt_f32_ubyte1_e32 v86, v24
	v_cvt_f32_ubyte2_e32 v87, v24
	v_cvt_f32_ubyte3_e32 v88, v24
	v_fmac_f32_e32 v2, v85, v53
	v_fmac_f32_e32 v3, v86, v53
	v_fmac_f32_e32 v4, v87, v53
	v_fmac_f32_e32 v5, v88, v53
	v_cvt_f32_ubyte0_e32 v85, v25
	v_cvt_f32_ubyte1_e32 v86, v25
	v_cvt_f32_ubyte2_e32 v87, v25
	v_cvt_f32_ubyte3_e32 v88, v25
	v_fmac_f32_e32 v6, v85, v53
	v_fmac_f32_e32 v7, v86, v53
	v_fmac_f32_e32 v8, v87, v53
	v_fmac_f32_e32 v9, v88, v53
	v_cvt_f32_ubyte0_e32 v85, v26
	v_cvt_f32_ubyte1_e32 v86, v26
	v_cvt_f32_ubyte2_e32 v87, v26
	v_cvt_f32_ubyte3_e32 v88, v26
	v_fmac_f32_e32 v10, v85, v53
	v_fmac_f32_e32 v11, v86, v53
	v_fmac_f32_e32 v12, v87, v53
	v_fmac_f32_e32 v13, v88, v53
	v_cvt_f32_ubyte0_e32 v85, v27
	v_cvt_f32_ubyte1_e32 v86, v27
	v_cvt_f32_ubyte2_e32 v87, v27
	v_cvt_f32_ubyte3_e32 v88, v27
	v_fmac_f32_e32 v14, v85, v53
	v_fmac_f32_e32 v15, v86, v53
	v_fmac_f32_e32 v16, v87, v53
	v_fmac_f32_e32 v17, v88, v53
	v_add_f32_e32 v18, v18, v53
	v_lshrrev_b32_e32 v84, 16, v79
	v_lshl_or_b32 v83, v84, 7, v89
	v_cmp_lt_i32_e32 vcc, 5, v78
	s_mov_b64 exec, vcc
	global_load_dwordx4 v[24:27], v83, s[12:13]
	s_mov_b64 exec, -1
	v_lshlrev_b32_e32 v109, 1, v84
	global_load_ushort v53, v109, s[14:15]
	s_waitcnt lgkmcnt(0)
	ds_bpermute_b32 v79, v90, v73 offset:16
	s_waitcnt vmcnt(6)
	v_cvt_f32_f16_e32 v54, v54
	v_cvt_f32_ubyte0_e32 v85, v28
	v_cvt_f32_ubyte1_e32 v86, v28
	v_cvt_f32_ubyte2_e32 v87, v28
	v_cvt_f32_ubyte3_e32 v88, v28
	v_fmac_f32_e32 v2, v85, v54
	v_fmac_f32_e32 v3, v86, v54
	v_fmac_f32_e32 v4, v87, v54
	v_fmac_f32_e32 v5, v88, v54
	v_cvt_f32_ubyte0_e32 v85, v29
	v_cvt_f32_ubyte1_e32 v86, v29
	v_cvt_f32_ubyte2_e32 v87, v29
	v_cvt_f32_ubyte3_e32 v88, v29
	v_fmac_f32_e32 v6, v85, v54
	v_fmac_f32_e32 v7, v86, v54
	v_fmac_f32_e32 v8, v87, v54
	v_fmac_f32_e32 v9, v88, v54
	v_cvt_f32_ubyte0_e32 v85, v30
	v_cvt_f32_ubyte1_e32 v86, v30
	v_cvt_f32_ubyte2_e32 v87, v30
	v_cvt_f32_ubyte3_e32 v88, v30
	v_fmac_f32_e32 v10, v85, v54
	v_fmac_f32_e32 v11, v86, v54
	v_fmac_f32_e32 v12, v87, v54
	v_fmac_f32_e32 v13, v88, v54
	v_cvt_f32_ubyte0_e32 v85, v31
	v_cvt_f32_ubyte1_e32 v86, v31
	v_cvt_f32_ubyte2_e32 v87, v31
	v_cvt_f32_ubyte3_e32 v88, v31
	v_fmac_f32_e32 v14, v85, v54
	v_fmac_f32_e32 v15, v86, v54
	v_fmac_f32_e32 v16, v87, v54
	v_fmac_f32_e32 v17, v88, v54
	v_add_f32_e32 v18, v18, v54
	v_and_b32_e32 v84, 0xffff, v80
	v_lshl_or_b32 v83, v84, 7, v89
	v_cmp_lt_i32_e32 vcc, 6, v78
	s_mov_b64 exec, vcc
	global_load_dwordx4 v[28:31], v83, s[12:13]
	s_mov_b64 exec, -1
	v_lshlrev_b32_e32 v109, 1, v84
	global_load_ushort v54, v109, s[14:15]
	s_waitcnt vmcnt(6)
	v_cvt_f32_f16_e32 v55, v55
	v_cvt_f32_ubyte0_e32 v85, v32
	v_cvt_f32_ubyte1_e32 v86, v32
	v_cvt_f32_ubyte2_e32 v87, v32
	v_cvt_f32_ubyte3_e32 v88, v32
	v_fmac_f32_e32 v2, v85, v55
	v_fmac_f32_e32 v3, v86, v55
	v_fmac_f32_e32 v4, v87, v55
	v_fmac_f32_e32 v5, v88, v55
	v_cvt_f32_ubyte0_e32 v85, v33
	v_cvt_f32_ubyte1_e32 v86, v33
	v_cvt_f32_ubyte2_e32 v87, v33
	v_cvt_f32_ubyte3_e32 v88, v33
	v_fmac_f32_e32 v6, v85, v55
	v_fmac_f32_e32 v7, v86, v55
	v_fmac_f32_e32 v8, v87, v55
	v_fmac_f32_e32 v9, v88, v55
	v_cvt_f32_ubyte0_e32 v85, v34
	v_cvt_f32_ubyte1_e32 v86, v34
	v_cvt_f32_ubyte2_e32 v87, v34
	v_cvt_f32_ubyte3_e32 v88, v34
	v_fmac_f32_e32 v10, v85, v55
	v_fmac_f32_e32 v11, v86, v55
	v_fmac_f32_e32 v12, v87, v55
	v_fmac_f32_e32 v13, v88, v55
	v_cvt_f32_ubyte0_e32 v85, v35
	v_cvt_f32_ubyte1_e32 v86, v35
	v_cvt_f32_ubyte2_e32 v87, v35
	v_cvt_f32_ubyte3_e32 v88, v35
	v_fmac_f32_e32 v14, v85, v55
	v_fmac_f32_e32 v15, v86, v55
	v_fmac_f32_e32 v16, v87, v55
	v_fmac_f32_e32 v17, v88, v55
	v_add_f32_e32 v18, v18, v55
	v_lshrrev_b32_e32 v84, 16, v80
	v_lshl_or_b32 v83, v84, 7, v89
	v_cmp_lt_i32_e32 vcc, 7, v78
	s_mov_b64 exec, vcc
	global_load_dwordx4 v[32:35], v83, s[12:13]
	s_mov_b64 exec, -1
	v_lshlrev_b32_e32 v109, 1, v84
	global_load_ushort v55, v109, s[14:15]
	s_cmp_le_u32 s40, 8
	s_cbranch_scc1 .Lg1_tail0
	s_waitcnt lgkmcnt(0)
	ds_bpermute_b32 v80, v90, v73 offset:20
	s_waitcnt vmcnt(6)
	v_cvt_f32_f16_e32 v52, v52
	v_cvt_f32_ubyte0_e32 v85, v20
	v_cvt_f32_ubyte1_e32 v86, v20
	v_cvt_f32_ubyte2_e32 v87, v20
	v_cvt_f32_ubyte3_e32 v88, v20
	v_fmac_f32_e32 v2, v85, v52
	v_fmac_f32_e32 v3, v86, v52
	v_fmac_f32_e32 v4, v87, v52
	v_fmac_f32_e32 v5, v88, v52
	v_cvt_f32_ubyte0_e32 v85, v21
	v_cvt_f32_ubyte1_e32 v86, v21
	v_cvt_f32_ubyte2_e32 v87, v21
	v_cvt_f32_ubyte3_e32 v88, v21
	v_fmac_f32_e32 v6, v85, v52
	v_fmac_f32_e32 v7, v86, v52
	v_fmac_f32_e32 v8, v87, v52
	v_fmac_f32_e32 v9, v88, v52
	v_cvt_f32_ubyte0_e32 v85, v22
	v_cvt_f32_ubyte1_e32 v86, v22
	v_cvt_f32_ubyte2_e32 v87, v22
	v_cvt_f32_ubyte3_e32 v88, v22
	v_fmac_f32_e32 v10, v85, v52
	v_fmac_f32_e32 v11, v86, v52
	v_fmac_f32_e32 v12, v87, v52
	v_fmac_f32_e32 v13, v88, v52
	v_cvt_f32_ubyte0_e32 v85, v23
	v_cvt_f32_ubyte1_e32 v86, v23
	v_cvt_f32_ubyte2_e32 v87, v23
	v_cvt_f32_ubyte3_e32 v88, v23
	v_fmac_f32_e32 v14, v85, v52
	v_fmac_f32_e32 v15, v86, v52
	v_fmac_f32_e32 v16, v87, v52
	v_fmac_f32_e32 v17, v88, v52
	v_add_f32_e32 v18, v18, v52
	v_and_b32_e32 v84, 0xffff, v79
	v_lshl_or_b32 v83, v84, 7, v89
	v_cmp_lt_i32_e32 vcc, 8, v78
	s_mov_b64 exec, vcc
	global_load_dwordx4 v[20:23], v83, s[12:13]
	s_mov_b64 exec, -1
	v_lshlrev_b32_e32 v109, 1, v84
	global_load_ushort v52, v109, s[14:15]
	s_waitcnt vmcnt(6)
	v_cvt_f32_f16_e32 v53, v53
	v_cvt_f32_ubyte0_e32 v85, v24
	v_cvt_f32_ubyte1_e32 v86, v24
	v_cvt_f32_ubyte2_e32 v87, v24
	v_cvt_f32_ubyte3_e32 v88, v24
	v_fmac_f32_e32 v2, v85, v53
	v_fmac_f32_e32 v3, v86, v53
	v_fmac_f32_e32 v4, v87, v53
	v_fmac_f32_e32 v5, v88, v53
	v_cvt_f32_ubyte0_e32 v85, v25
	v_cvt_f32_ubyte1_e32 v86, v25
	v_cvt_f32_ubyte2_e32 v87, v25
	v_cvt_f32_ubyte3_e32 v88, v25
	v_fmac_f32_e32 v6, v85, v53
	v_fmac_f32_e32 v7, v86, v53
	v_fmac_f32_e32 v8, v87, v53
	v_fmac_f32_e32 v9, v88, v53
	v_cvt_f32_ubyte0_e32 v85, v26
	v_cvt_f32_ubyte1_e32 v86, v26
	v_cvt_f32_ubyte2_e32 v87, v26
	v_cvt_f32_ubyte3_e32 v88, v26
	v_fmac_f32_e32 v10, v85, v53
	v_fmac_f32_e32 v11, v86, v53
	v_fmac_f32_e32 v12, v87, v53
	v_fmac_f32_e32 v13, v88, v53
	v_cvt_f32_ubyte0_e32 v85, v27
	v_cvt_f32_ubyte1_e32 v86, v27
	v_cvt_f32_ubyte2_e32 v87, v27
	v_cvt_f32_ubyte3_e32 v88, v27
	v_fmac_f32_e32 v14, v85, v53
	v_fmac_f32_e32 v15, v86, v53
	v_fmac_f32_e32 v16, v87, v53
	v_fmac_f32_e32 v17, v88, v53
	v_add_f32_e32 v18, v18, v53
	v_lshrrev_b32_e32 v84, 16, v79
	v_lshl_or_b32 v83, v84, 7, v89
	v_cmp_lt_i32_e32 vcc, 9, v78
	s_mov_b64 exec, vcc
	global_load_dwordx4 v[24:27], v83, s[12:13]
	s_mov_b64 exec, -1
	v_lshlrev_b32_e32 v109, 1, v84
	global_load_ushort v53, v109, s[14:15]
	s_waitcnt lgkmcnt(0)
	ds_bpermute_b32 v79, v90, v73 offset:24
	s_waitcnt vmcnt(6)
	v_cvt_f32_f16_e32 v54, v54
	v_cvt_f32_ubyte0_e32 v85, v28
	v_cvt_f32_ubyte1_e32 v86, v28
	v_cvt_f32_ubyte2_e32 v87, v28
	v_cvt_f32_ubyte3_e32 v88, v28
	v_fmac_f32_e32 v2, v85, v54
	v_fmac_f32_e32 v3, v86, v54
	v_fmac_f32_e32 v4, v87, v54
	v_fmac_f32_e32 v5, v88, v54
	v_cvt_f32_ubyte0_e32 v85, v29
	v_cvt_f32_ubyte1_e32 v86, v29
	v_cvt_f32_ubyte2_e32 v87, v29
	v_cvt_f32_ubyte3_e32 v88, v29
	v_fmac_f32_e32 v6, v85, v54
	v_fmac_f32_e32 v7, v86, v54
	v_fmac_f32_e32 v8, v87, v54
	v_fmac_f32_e32 v9, v88, v54
	v_cvt_f32_ubyte0_e32 v85, v30
	v_cvt_f32_ubyte1_e32 v86, v30
	v_cvt_f32_ubyte2_e32 v87, v30
	v_cvt_f32_ubyte3_e32 v88, v30
	v_fmac_f32_e32 v10, v85, v54
	v_fmac_f32_e32 v11, v86, v54
	v_fmac_f32_e32 v12, v87, v54
	v_fmac_f32_e32 v13, v88, v54
	v_cvt_f32_ubyte0_e32 v85, v31
	v_cvt_f32_ubyte1_e32 v86, v31
	v_cvt_f32_ubyte2_e32 v87, v31
	v_cvt_f32_ubyte3_e32 v88, v31
	v_fmac_f32_e32 v14, v85, v54
	v_fmac_f32_e32 v15, v86, v54
	v_fmac_f32_e32 v16, v87, v54
	v_fmac_f32_e32 v17, v88, v54
	v_add_f32_e32 v18, v18, v54
	v_and_b32_e32 v84, 0xffff, v80
	v_lshl_or_b32 v83, v84, 7, v89
	v_cmp_lt_i32_e32 vcc, 10, v78
	s_mov_b64 exec, vcc
	global_load_dwordx4 v[28:31], v83, s[12:13]
	s_mov_b64 exec, -1
	v_lshlrev_b32_e32 v109, 1, v84
	global_load_ushort v54, v109, s[14:15]
	s_waitcnt vmcnt(6)
	v_cvt_f32_f16_e32 v55, v55
	v_cvt_f32_ubyte0_e32 v85, v32
	v_cvt_f32_ubyte1_e32 v86, v32
	v_cvt_f32_ubyte2_e32 v87, v32
	v_cvt_f32_ubyte3_e32 v88, v32
	v_fmac_f32_e32 v2, v85, v55
	v_fmac_f32_e32 v3, v86, v55
	v_fmac_f32_e32 v4, v87, v55
	v_fmac_f32_e32 v5, v88, v55
	v_cvt_f32_ubyte0_e32 v85, v33
	v_cvt_f32_ubyte1_e32 v86, v33
	v_cvt_f32_ubyte2_e32 v87, v33
	v_cvt_f32_ubyte3_e32 v88, v33
	v_fmac_f32_e32 v6, v85, v55
	v_fmac_f32_e32 v7, v86, v55
	v_fmac_f32_e32 v8, v87, v55
	v_fmac_f32_e32 v9, v88, v55
	v_cvt_f32_ubyte0_e32 v85, v34
	v_cvt_f32_ubyte1_e32 v86, v34
	v_cvt_f32_ubyte2_e32 v87, v34
	v_cvt_f32_ubyte3_e32 v88, v34
	v_fmac_f32_e32 v10, v85, v55
	v_fmac_f32_e32 v11, v86, v55
	v_fmac_f32_e32 v12, v87, v55
	v_fmac_f32_e32 v13, v88, v55
	v_cvt_f32_ubyte0_e32 v85, v35
	v_cvt_f32_ubyte1_e32 v86, v35
	v_cvt_f32_ubyte2_e32 v87, v35
	v_cvt_f32_ubyte3_e32 v88, v35
	v_fmac_f32_e32 v14, v85, v55
	v_fmac_f32_e32 v15, v86, v55
	v_fmac_f32_e32 v16, v87, v55
	v_fmac_f32_e32 v17, v88, v55
	v_add_f32_e32 v18, v18, v55
	v_lshrrev_b32_e32 v84, 16, v80
	v_lshl_or_b32 v83, v84, 7, v89
	v_cmp_lt_i32_e32 vcc, 11, v78
	s_mov_b64 exec, vcc
	global_load_dwordx4 v[32:35], v83, s[12:13]
	s_mov_b64 exec, -1
	v_lshlrev_b32_e32 v109, 1, v84
	global_load_ushort v55, v109, s[14:15]
	s_cmp_le_u32 s40, 12
	s_cbranch_scc1 .Lg1_tail0
	s_waitcnt lgkmcnt(0)
	ds_bpermute_b32 v80, v90, v73 offset:28
	s_waitcnt vmcnt(6)
	v_cvt_f32_f16_e32 v52, v52
	v_cvt_f32_ubyte0_e32 v85, v20
	v_cvt_f32_ubyte1_e32 v86, v20
	v_cvt_f32_ubyte2_e32 v87, v20
	v_cvt_f32_ubyte3_e32 v88, v20
	v_fmac_f32_e32 v2, v85, v52
	v_fmac_f32_e32 v3, v86, v52
	v_fmac_f32_e32 v4, v87, v52
	v_fmac_f32_e32 v5, v88, v52
	v_cvt_f32_ubyte0_e32 v85, v21
	v_cvt_f32_ubyte1_e32 v86, v21
	v_cvt_f32_ubyte2_e32 v87, v21
	v_cvt_f32_ubyte3_e32 v88, v21
	v_fmac_f32_e32 v6, v85, v52
	v_fmac_f32_e32 v7, v86, v52
	v_fmac_f32_e32 v8, v87, v52
	v_fmac_f32_e32 v9, v88, v52
	v_cvt_f32_ubyte0_e32 v85, v22
	v_cvt_f32_ubyte1_e32 v86, v22
	v_cvt_f32_ubyte2_e32 v87, v22
	v_cvt_f32_ubyte3_e32 v88, v22
	v_fmac_f32_e32 v10, v85, v52
	v_fmac_f32_e32 v11, v86, v52
	v_fmac_f32_e32 v12, v87, v52
	v_fmac_f32_e32 v13, v88, v52
	v_cvt_f32_ubyte0_e32 v85, v23
	v_cvt_f32_ubyte1_e32 v86, v23
	v_cvt_f32_ubyte2_e32 v87, v23
	v_cvt_f32_ubyte3_e32 v88, v23
	v_fmac_f32_e32 v14, v85, v52
	v_fmac_f32_e32 v15, v86, v52
	v_fmac_f32_e32 v16, v87, v52
	v_fmac_f32_e32 v17, v88, v52
	v_add_f32_e32 v18, v18, v52
	v_and_b32_e32 v84, 0xffff, v79
	v_lshl_or_b32 v83, v84, 7, v89
	v_cmp_lt_i32_e32 vcc, 12, v78
	s_mov_b64 exec, vcc
	global_load_dwordx4 v[20:23], v83, s[12:13]
	s_mov_b64 exec, -1
	v_lshlrev_b32_e32 v109, 1, v84
	global_load_ushort v52, v109, s[14:15]
	s_waitcnt vmcnt(6)
	v_cvt_f32_f16_e32 v53, v53
	v_cvt_f32_ubyte0_e32 v85, v24
	v_cvt_f32_ubyte1_e32 v86, v24
	v_cvt_f32_ubyte2_e32 v87, v24
	v_cvt_f32_ubyte3_e32 v88, v24
	v_fmac_f32_e32 v2, v85, v53
	v_fmac_f32_e32 v3, v86, v53
	v_fmac_f32_e32 v4, v87, v53
	v_fmac_f32_e32 v5, v88, v53
	v_cvt_f32_ubyte0_e32 v85, v25
	v_cvt_f32_ubyte1_e32 v86, v25
	v_cvt_f32_ubyte2_e32 v87, v25
	v_cvt_f32_ubyte3_e32 v88, v25
	v_fmac_f32_e32 v6, v85, v53
	v_fmac_f32_e32 v7, v86, v53
	v_fmac_f32_e32 v8, v87, v53
	v_fmac_f32_e32 v9, v88, v53
	v_cvt_f32_ubyte0_e32 v85, v26
	v_cvt_f32_ubyte1_e32 v86, v26
	v_cvt_f32_ubyte2_e32 v87, v26
	v_cvt_f32_ubyte3_e32 v88, v26
	v_fmac_f32_e32 v10, v85, v53
	v_fmac_f32_e32 v11, v86, v53
	v_fmac_f32_e32 v12, v87, v53
	v_fmac_f32_e32 v13, v88, v53
	v_cvt_f32_ubyte0_e32 v85, v27
	v_cvt_f32_ubyte1_e32 v86, v27
	v_cvt_f32_ubyte2_e32 v87, v27
	v_cvt_f32_ubyte3_e32 v88, v27
	v_fmac_f32_e32 v14, v85, v53
	v_fmac_f32_e32 v15, v86, v53
	v_fmac_f32_e32 v16, v87, v53
	v_fmac_f32_e32 v17, v88, v53
	v_add_f32_e32 v18, v18, v53
	v_lshrrev_b32_e32 v84, 16, v79
	v_lshl_or_b32 v83, v84, 7, v89
	v_cmp_lt_i32_e32 vcc, 13, v78
	s_mov_b64 exec, vcc
	global_load_dwordx4 v[24:27], v83, s[12:13]
	s_mov_b64 exec, -1
	v_lshlrev_b32_e32 v109, 1, v84
	global_load_ushort v53, v109, s[14:15]
	s_waitcnt lgkmcnt(0)
	ds_bpermute_b32 v79, v90, v74 offset:0
	s_waitcnt vmcnt(6)
	v_cvt_f32_f16_e32 v54, v54
	v_cvt_f32_ubyte0_e32 v85, v28
	v_cvt_f32_ubyte1_e32 v86, v28
	v_cvt_f32_ubyte2_e32 v87, v28
	v_cvt_f32_ubyte3_e32 v88, v28
	v_fmac_f32_e32 v2, v85, v54
	v_fmac_f32_e32 v3, v86, v54
	v_fmac_f32_e32 v4, v87, v54
	v_fmac_f32_e32 v5, v88, v54
	v_cvt_f32_ubyte0_e32 v85, v29
	v_cvt_f32_ubyte1_e32 v86, v29
	v_cvt_f32_ubyte2_e32 v87, v29
	v_cvt_f32_ubyte3_e32 v88, v29
	v_fmac_f32_e32 v6, v85, v54
	v_fmac_f32_e32 v7, v86, v54
	v_fmac_f32_e32 v8, v87, v54
	v_fmac_f32_e32 v9, v88, v54
	v_cvt_f32_ubyte0_e32 v85, v30
	v_cvt_f32_ubyte1_e32 v86, v30
	v_cvt_f32_ubyte2_e32 v87, v30
	v_cvt_f32_ubyte3_e32 v88, v30
	v_fmac_f32_e32 v10, v85, v54
	v_fmac_f32_e32 v11, v86, v54
	v_fmac_f32_e32 v12, v87, v54
	v_fmac_f32_e32 v13, v88, v54
	v_cvt_f32_ubyte0_e32 v85, v31
	v_cvt_f32_ubyte1_e32 v86, v31
	v_cvt_f32_ubyte2_e32 v87, v31
	v_cvt_f32_ubyte3_e32 v88, v31
	v_fmac_f32_e32 v14, v85, v54
	v_fmac_f32_e32 v15, v86, v54
	v_fmac_f32_e32 v16, v87, v54
	v_fmac_f32_e32 v17, v88, v54
	v_add_f32_e32 v18, v18, v54
	v_and_b32_e32 v84, 0xffff, v80
	v_lshl_or_b32 v83, v84, 7, v89
	v_cmp_lt_i32_e32 vcc, 14, v78
	s_mov_b64 exec, vcc
	global_load_dwordx4 v[28:31], v83, s[12:13]
	s_mov_b64 exec, -1
	v_lshlrev_b32_e32 v109, 1, v84
	global_load_ushort v54, v109, s[14:15]
	s_waitcnt vmcnt(6)
	v_cvt_f32_f16_e32 v55, v55
	v_cvt_f32_ubyte0_e32 v85, v32
	v_cvt_f32_ubyte1_e32 v86, v32
	v_cvt_f32_ubyte2_e32 v87, v32
	v_cvt_f32_ubyte3_e32 v88, v32
	v_fmac_f32_e32 v2, v85, v55
	v_fmac_f32_e32 v3, v86, v55
	v_fmac_f32_e32 v4, v87, v55
	v_fmac_f32_e32 v5, v88, v55
	v_cvt_f32_ubyte0_e32 v85, v33
	v_cvt_f32_ubyte1_e32 v86, v33
	v_cvt_f32_ubyte2_e32 v87, v33
	v_cvt_f32_ubyte3_e32 v88, v33
	v_fmac_f32_e32 v6, v85, v55
	v_fmac_f32_e32 v7, v86, v55
	v_fmac_f32_e32 v8, v87, v55
	v_fmac_f32_e32 v9, v88, v55
	v_cvt_f32_ubyte0_e32 v85, v34
	v_cvt_f32_ubyte1_e32 v86, v34
	v_cvt_f32_ubyte2_e32 v87, v34
	v_cvt_f32_ubyte3_e32 v88, v34
	v_fmac_f32_e32 v10, v85, v55
	v_fmac_f32_e32 v11, v86, v55
	v_fmac_f32_e32 v12, v87, v55
	v_fmac_f32_e32 v13, v88, v55
	v_cvt_f32_ubyte0_e32 v85, v35
	v_cvt_f32_ubyte1_e32 v86, v35
	v_cvt_f32_ubyte2_e32 v87, v35
	v_cvt_f32_ubyte3_e32 v88, v35
	v_fmac_f32_e32 v14, v85, v55
	v_fmac_f32_e32 v15, v86, v55
	v_fmac_f32_e32 v16, v87, v55
	v_fmac_f32_e32 v17, v88, v55
	v_add_f32_e32 v18, v18, v55
	v_lshrrev_b32_e32 v84, 16, v80
	v_lshl_or_b32 v83, v84, 7, v89
	v_cmp_lt_i32_e32 vcc, 15, v78
	s_mov_b64 exec, vcc
	global_load_dwordx4 v[32:35], v83, s[12:13]
	s_mov_b64 exec, -1
	v_lshlrev_b32_e32 v109, 1, v84
	global_load_ushort v55, v109, s[14:15]
	s_cmp_le_u32 s40, 16
	s_cbranch_scc1 .Lg1_tail0
	s_waitcnt lgkmcnt(0)
	ds_bpermute_b32 v80, v90, v74 offset:4
	s_waitcnt vmcnt(6)
	v_cvt_f32_f16_e32 v52, v52
	v_cvt_f32_ubyte0_e32 v85, v20
	v_cvt_f32_ubyte1_e32 v86, v20
	v_cvt_f32_ubyte2_e32 v87, v20
	v_cvt_f32_ubyte3_e32 v88, v20
	v_fmac_f32_e32 v2, v85, v52
	v_fmac_f32_e32 v3, v86, v52
	v_fmac_f32_e32 v4, v87, v52
	v_fmac_f32_e32 v5, v88, v52
	v_cvt_f32_ubyte0_e32 v85, v21
	v_cvt_f32_ubyte1_e32 v86, v21
	v_cvt_f32_ubyte2_e32 v87, v21
	v_cvt_f32_ubyte3_e32 v88, v21
	v_fmac_f32_e32 v6, v85, v52
	v_fmac_f32_e32 v7, v86, v52
	v_fmac_f32_e32 v8, v87, v52
	v_fmac_f32_e32 v9, v88, v52
	v_cvt_f32_ubyte0_e32 v85, v22
	v_cvt_f32_ubyte1_e32 v86, v22
	v_cvt_f32_ubyte2_e32 v87, v22
	v_cvt_f32_ubyte3_e32 v88, v22
	v_fmac_f32_e32 v10, v85, v52
	v_fmac_f32_e32 v11, v86, v52
	v_fmac_f32_e32 v12, v87, v52
	v_fmac_f32_e32 v13, v88, v52
	v_cvt_f32_ubyte0_e32 v85, v23
	v_cvt_f32_ubyte1_e32 v86, v23
	v_cvt_f32_ubyte2_e32 v87, v23
	v_cvt_f32_ubyte3_e32 v88, v23
	v_fmac_f32_e32 v14, v85, v52
	v_fmac_f32_e32 v15, v86, v52
	v_fmac_f32_e32 v16, v87, v52
	v_fmac_f32_e32 v17, v88, v52
	v_add_f32_e32 v18, v18, v52
	v_and_b32_e32 v84, 0xffff, v79
	v_lshl_or_b32 v83, v84, 7, v89
	v_cmp_lt_i32_e32 vcc, 16, v78
	s_mov_b64 exec, vcc
	global_load_dwordx4 v[20:23], v83, s[12:13]
	s_mov_b64 exec, -1
	v_lshlrev_b32_e32 v109, 1, v84
	global_load_ushort v52, v109, s[14:15]
	s_waitcnt vmcnt(6)
	v_cvt_f32_f16_e32 v53, v53
	v_cvt_f32_ubyte0_e32 v85, v24
	v_cvt_f32_ubyte1_e32 v86, v24
	v_cvt_f32_ubyte2_e32 v87, v24
	v_cvt_f32_ubyte3_e32 v88, v24
	v_fmac_f32_e32 v2, v85, v53
	v_fmac_f32_e32 v3, v86, v53
	v_fmac_f32_e32 v4, v87, v53
	v_fmac_f32_e32 v5, v88, v53
	v_cvt_f32_ubyte0_e32 v85, v25
	v_cvt_f32_ubyte1_e32 v86, v25
	v_cvt_f32_ubyte2_e32 v87, v25
	v_cvt_f32_ubyte3_e32 v88, v25
	v_fmac_f32_e32 v6, v85, v53
	v_fmac_f32_e32 v7, v86, v53
	v_fmac_f32_e32 v8, v87, v53
	v_fmac_f32_e32 v9, v88, v53
	v_cvt_f32_ubyte0_e32 v85, v26
	v_cvt_f32_ubyte1_e32 v86, v26
	v_cvt_f32_ubyte2_e32 v87, v26
	v_cvt_f32_ubyte3_e32 v88, v26
	v_fmac_f32_e32 v10, v85, v53
	v_fmac_f32_e32 v11, v86, v53
	v_fmac_f32_e32 v12, v87, v53
	v_fmac_f32_e32 v13, v88, v53
	v_cvt_f32_ubyte0_e32 v85, v27
	v_cvt_f32_ubyte1_e32 v86, v27
	v_cvt_f32_ubyte2_e32 v87, v27
	v_cvt_f32_ubyte3_e32 v88, v27
	v_fmac_f32_e32 v14, v85, v53
	v_fmac_f32_e32 v15, v86, v53
	v_fmac_f32_e32 v16, v87, v53
	v_fmac_f32_e32 v17, v88, v53
	v_add_f32_e32 v18, v18, v53
	v_lshrrev_b32_e32 v84, 16, v79
	v_lshl_or_b32 v83, v84, 7, v89
	v_cmp_lt_i32_e32 vcc, 17, v78
	s_mov_b64 exec, vcc
	global_load_dwordx4 v[24:27], v83, s[12:13]
	s_mov_b64 exec, -1
	v_lshlrev_b32_e32 v109, 1, v84
	global_load_ushort v53, v109, s[14:15]
	s_waitcnt lgkmcnt(0)
	ds_bpermute_b32 v79, v90, v74 offset:8
	s_waitcnt vmcnt(6)
	v_cvt_f32_f16_e32 v54, v54
	v_cvt_f32_ubyte0_e32 v85, v28
	v_cvt_f32_ubyte1_e32 v86, v28
	v_cvt_f32_ubyte2_e32 v87, v28
	v_cvt_f32_ubyte3_e32 v88, v28
	v_fmac_f32_e32 v2, v85, v54
	v_fmac_f32_e32 v3, v86, v54
	v_fmac_f32_e32 v4, v87, v54
	v_fmac_f32_e32 v5, v88, v54
	v_cvt_f32_ubyte0_e32 v85, v29
	v_cvt_f32_ubyte1_e32 v86, v29
	v_cvt_f32_ubyte2_e32 v87, v29
	v_cvt_f32_ubyte3_e32 v88, v29
	v_fmac_f32_e32 v6, v85, v54
	v_fmac_f32_e32 v7, v86, v54
	v_fmac_f32_e32 v8, v87, v54
	v_fmac_f32_e32 v9, v88, v54
	v_cvt_f32_ubyte0_e32 v85, v30
	v_cvt_f32_ubyte1_e32 v86, v30
	v_cvt_f32_ubyte2_e32 v87, v30
	v_cvt_f32_ubyte3_e32 v88, v30
	v_fmac_f32_e32 v10, v85, v54
	v_fmac_f32_e32 v11, v86, v54
	v_fmac_f32_e32 v12, v87, v54
	v_fmac_f32_e32 v13, v88, v54
	v_cvt_f32_ubyte0_e32 v85, v31
	v_cvt_f32_ubyte1_e32 v86, v31
	v_cvt_f32_ubyte2_e32 v87, v31
	v_cvt_f32_ubyte3_e32 v88, v31
	v_fmac_f32_e32 v14, v85, v54
	v_fmac_f32_e32 v15, v86, v54
	v_fmac_f32_e32 v16, v87, v54
	v_fmac_f32_e32 v17, v88, v54
	v_add_f32_e32 v18, v18, v54
	v_and_b32_e32 v84, 0xffff, v80
	v_lshl_or_b32 v83, v84, 7, v89
	v_cmp_lt_i32_e32 vcc, 18, v78
	s_mov_b64 exec, vcc
	global_load_dwordx4 v[28:31], v83, s[12:13]
	s_mov_b64 exec, -1
	v_lshlrev_b32_e32 v109, 1, v84
	global_load_ushort v54, v109, s[14:15]
	s_waitcnt vmcnt(6)
	v_cvt_f32_f16_e32 v55, v55
	v_cvt_f32_ubyte0_e32 v85, v32
	v_cvt_f32_ubyte1_e32 v86, v32
	v_cvt_f32_ubyte2_e32 v87, v32
	v_cvt_f32_ubyte3_e32 v88, v32
	v_fmac_f32_e32 v2, v85, v55
	v_fmac_f32_e32 v3, v86, v55
	v_fmac_f32_e32 v4, v87, v55
	v_fmac_f32_e32 v5, v88, v55
	v_cvt_f32_ubyte0_e32 v85, v33
	v_cvt_f32_ubyte1_e32 v86, v33
	v_cvt_f32_ubyte2_e32 v87, v33
	v_cvt_f32_ubyte3_e32 v88, v33
	v_fmac_f32_e32 v6, v85, v55
	v_fmac_f32_e32 v7, v86, v55
	v_fmac_f32_e32 v8, v87, v55
	v_fmac_f32_e32 v9, v88, v55
	v_cvt_f32_ubyte0_e32 v85, v34
	v_cvt_f32_ubyte1_e32 v86, v34
	v_cvt_f32_ubyte2_e32 v87, v34
	v_cvt_f32_ubyte3_e32 v88, v34
	v_fmac_f32_e32 v10, v85, v55
	v_fmac_f32_e32 v11, v86, v55
	v_fmac_f32_e32 v12, v87, v55
	v_fmac_f32_e32 v13, v88, v55
	v_cvt_f32_ubyte0_e32 v85, v35
	v_cvt_f32_ubyte1_e32 v86, v35
	v_cvt_f32_ubyte2_e32 v87, v35
	v_cvt_f32_ubyte3_e32 v88, v35
	v_fmac_f32_e32 v14, v85, v55
	v_fmac_f32_e32 v15, v86, v55
	v_fmac_f32_e32 v16, v87, v55
	v_fmac_f32_e32 v17, v88, v55
	v_add_f32_e32 v18, v18, v55
	v_lshrrev_b32_e32 v84, 16, v80
	v_lshl_or_b32 v83, v84, 7, v89
	v_cmp_lt_i32_e32 vcc, 19, v78
	s_mov_b64 exec, vcc
	global_load_dwordx4 v[32:35], v83, s[12:13]
	s_mov_b64 exec, -1
	v_lshlrev_b32_e32 v109, 1, v84
	global_load_ushort v55, v109, s[14:15]
	s_cmp_le_u32 s40, 20
	s_cbranch_scc1 .Lg1_tail0
	s_waitcnt lgkmcnt(0)
	ds_bpermute_b32 v80, v90, v74 offset:12
	s_waitcnt vmcnt(6)
	v_cvt_f32_f16_e32 v52, v52
	v_cvt_f32_ubyte0_e32 v85, v20
	v_cvt_f32_ubyte1_e32 v86, v20
	v_cvt_f32_ubyte2_e32 v87, v20
	v_cvt_f32_ubyte3_e32 v88, v20
	v_fmac_f32_e32 v2, v85, v52
	v_fmac_f32_e32 v3, v86, v52
	v_fmac_f32_e32 v4, v87, v52
	v_fmac_f32_e32 v5, v88, v52
	v_cvt_f32_ubyte0_e32 v85, v21
	v_cvt_f32_ubyte1_e32 v86, v21
	v_cvt_f32_ubyte2_e32 v87, v21
	v_cvt_f32_ubyte3_e32 v88, v21
	v_fmac_f32_e32 v6, v85, v52
	v_fmac_f32_e32 v7, v86, v52
	v_fmac_f32_e32 v8, v87, v52
	v_fmac_f32_e32 v9, v88, v52
	v_cvt_f32_ubyte0_e32 v85, v22
	v_cvt_f32_ubyte1_e32 v86, v22
	v_cvt_f32_ubyte2_e32 v87, v22
	v_cvt_f32_ubyte3_e32 v88, v22
	v_fmac_f32_e32 v10, v85, v52
	v_fmac_f32_e32 v11, v86, v52
	v_fmac_f32_e32 v12, v87, v52
	v_fmac_f32_e32 v13, v88, v52
	v_cvt_f32_ubyte0_e32 v85, v23
	v_cvt_f32_ubyte1_e32 v86, v23
	v_cvt_f32_ubyte2_e32 v87, v23
	v_cvt_f32_ubyte3_e32 v88, v23
	v_fmac_f32_e32 v14, v85, v52
	v_fmac_f32_e32 v15, v86, v52
	v_fmac_f32_e32 v16, v87, v52
	v_fmac_f32_e32 v17, v88, v52
	v_add_f32_e32 v18, v18, v52
	v_and_b32_e32 v84, 0xffff, v79
	v_lshl_or_b32 v83, v84, 7, v89
	v_cmp_lt_i32_e32 vcc, 20, v78
	s_mov_b64 exec, vcc
	global_load_dwordx4 v[20:23], v83, s[12:13]
	s_mov_b64 exec, -1
	v_lshlrev_b32_e32 v109, 1, v84
	global_load_ushort v52, v109, s[14:15]
	s_waitcnt vmcnt(6)
	v_cvt_f32_f16_e32 v53, v53
	v_cvt_f32_ubyte0_e32 v85, v24
	v_cvt_f32_ubyte1_e32 v86, v24
	v_cvt_f32_ubyte2_e32 v87, v24
	v_cvt_f32_ubyte3_e32 v88, v24
	v_fmac_f32_e32 v2, v85, v53
	v_fmac_f32_e32 v3, v86, v53
	v_fmac_f32_e32 v4, v87, v53
	v_fmac_f32_e32 v5, v88, v53
	v_cvt_f32_ubyte0_e32 v85, v25
	v_cvt_f32_ubyte1_e32 v86, v25
	v_cvt_f32_ubyte2_e32 v87, v25
	v_cvt_f32_ubyte3_e32 v88, v25
	v_fmac_f32_e32 v6, v85, v53
	v_fmac_f32_e32 v7, v86, v53
	v_fmac_f32_e32 v8, v87, v53
	v_fmac_f32_e32 v9, v88, v53
	v_cvt_f32_ubyte0_e32 v85, v26
	v_cvt_f32_ubyte1_e32 v86, v26
	v_cvt_f32_ubyte2_e32 v87, v26
	v_cvt_f32_ubyte3_e32 v88, v26
	v_fmac_f32_e32 v10, v85, v53
	v_fmac_f32_e32 v11, v86, v53
	v_fmac_f32_e32 v12, v87, v53
	v_fmac_f32_e32 v13, v88, v53
	v_cvt_f32_ubyte0_e32 v85, v27
	v_cvt_f32_ubyte1_e32 v86, v27
	v_cvt_f32_ubyte2_e32 v87, v27
	v_cvt_f32_ubyte3_e32 v88, v27
	v_fmac_f32_e32 v14, v85, v53
	v_fmac_f32_e32 v15, v86, v53
	v_fmac_f32_e32 v16, v87, v53
	v_fmac_f32_e32 v17, v88, v53
	v_add_f32_e32 v18, v18, v53
	v_lshrrev_b32_e32 v84, 16, v79
	v_lshl_or_b32 v83, v84, 7, v89
	v_cmp_lt_i32_e32 vcc, 21, v78
	s_mov_b64 exec, vcc
	global_load_dwordx4 v[24:27], v83, s[12:13]
	s_mov_b64 exec, -1
	v_lshlrev_b32_e32 v109, 1, v84
	global_load_ushort v53, v109, s[14:15]
	s_waitcnt lgkmcnt(0)
	ds_bpermute_b32 v79, v90, v74 offset:16
	s_waitcnt vmcnt(6)
	v_cvt_f32_f16_e32 v54, v54
	v_cvt_f32_ubyte0_e32 v85, v28
	v_cvt_f32_ubyte1_e32 v86, v28
	v_cvt_f32_ubyte2_e32 v87, v28
	v_cvt_f32_ubyte3_e32 v88, v28
	v_fmac_f32_e32 v2, v85, v54
	v_fmac_f32_e32 v3, v86, v54
	v_fmac_f32_e32 v4, v87, v54
	v_fmac_f32_e32 v5, v88, v54
	v_cvt_f32_ubyte0_e32 v85, v29
	v_cvt_f32_ubyte1_e32 v86, v29
	v_cvt_f32_ubyte2_e32 v87, v29
	v_cvt_f32_ubyte3_e32 v88, v29
	v_fmac_f32_e32 v6, v85, v54
	v_fmac_f32_e32 v7, v86, v54
	v_fmac_f32_e32 v8, v87, v54
	v_fmac_f32_e32 v9, v88, v54
	v_cvt_f32_ubyte0_e32 v85, v30
	v_cvt_f32_ubyte1_e32 v86, v30
	v_cvt_f32_ubyte2_e32 v87, v30
	v_cvt_f32_ubyte3_e32 v88, v30
	v_fmac_f32_e32 v10, v85, v54
	v_fmac_f32_e32 v11, v86, v54
	v_fmac_f32_e32 v12, v87, v54
	v_fmac_f32_e32 v13, v88, v54
	v_cvt_f32_ubyte0_e32 v85, v31
	v_cvt_f32_ubyte1_e32 v86, v31
	v_cvt_f32_ubyte2_e32 v87, v31
	v_cvt_f32_ubyte3_e32 v88, v31
	v_fmac_f32_e32 v14, v85, v54
	v_fmac_f32_e32 v15, v86, v54
	v_fmac_f32_e32 v16, v87, v54
	v_fmac_f32_e32 v17, v88, v54
	v_add_f32_e32 v18, v18, v54
	v_and_b32_e32 v84, 0xffff, v80
	v_lshl_or_b32 v83, v84, 7, v89
	v_cmp_lt_i32_e32 vcc, 22, v78
	s_mov_b64 exec, vcc
	global_load_dwordx4 v[28:31], v83, s[12:13]
	s_mov_b64 exec, -1
	v_lshlrev_b32_e32 v109, 1, v84
	global_load_ushort v54, v109, s[14:15]
	s_waitcnt vmcnt(6)
	v_cvt_f32_f16_e32 v55, v55
	v_cvt_f32_ubyte0_e32 v85, v32
	v_cvt_f32_ubyte1_e32 v86, v32
	v_cvt_f32_ubyte2_e32 v87, v32
	v_cvt_f32_ubyte3_e32 v88, v32
	v_fmac_f32_e32 v2, v85, v55
	v_fmac_f32_e32 v3, v86, v55
	v_fmac_f32_e32 v4, v87, v55
	v_fmac_f32_e32 v5, v88, v55
	v_cvt_f32_ubyte0_e32 v85, v33
	v_cvt_f32_ubyte1_e32 v86, v33
	v_cvt_f32_ubyte2_e32 v87, v33
	v_cvt_f32_ubyte3_e32 v88, v33
	v_fmac_f32_e32 v6, v85, v55
	v_fmac_f32_e32 v7, v86, v55
	v_fmac_f32_e32 v8, v87, v55
	v_fmac_f32_e32 v9, v88, v55
	v_cvt_f32_ubyte0_e32 v85, v34
	v_cvt_f32_ubyte1_e32 v86, v34
	v_cvt_f32_ubyte2_e32 v87, v34
	v_cvt_f32_ubyte3_e32 v88, v34
	v_fmac_f32_e32 v10, v85, v55
	v_fmac_f32_e32 v11, v86, v55
	v_fmac_f32_e32 v12, v87, v55
	v_fmac_f32_e32 v13, v88, v55
	v_cvt_f32_ubyte0_e32 v85, v35
	v_cvt_f32_ubyte1_e32 v86, v35
	v_cvt_f32_ubyte2_e32 v87, v35
	v_cvt_f32_ubyte3_e32 v88, v35
	v_fmac_f32_e32 v14, v85, v55
	v_fmac_f32_e32 v15, v86, v55
	v_fmac_f32_e32 v16, v87, v55
	v_fmac_f32_e32 v17, v88, v55
	v_add_f32_e32 v18, v18, v55
	v_lshrrev_b32_e32 v84, 16, v80
	v_lshl_or_b32 v83, v84, 7, v89
	v_cmp_lt_i32_e32 vcc, 23, v78
	s_mov_b64 exec, vcc
	global_load_dwordx4 v[32:35], v83, s[12:13]
	s_mov_b64 exec, -1
	v_lshlrev_b32_e32 v109, 1, v84
	global_load_ushort v55, v109, s[14:15]
	s_cmp_le_u32 s40, 24
	s_cbranch_scc1 .Lg1_tail0
	s_waitcnt lgkmcnt(0)
	ds_bpermute_b32 v80, v90, v74 offset:20
	s_waitcnt vmcnt(6)
	v_cvt_f32_f16_e32 v52, v52
	v_cvt_f32_ubyte0_e32 v85, v20
	v_cvt_f32_ubyte1_e32 v86, v20
	v_cvt_f32_ubyte2_e32 v87, v20
	v_cvt_f32_ubyte3_e32 v88, v20
	v_fmac_f32_e32 v2, v85, v52
	v_fmac_f32_e32 v3, v86, v52
	v_fmac_f32_e32 v4, v87, v52
	v_fmac_f32_e32 v5, v88, v52
	v_cvt_f32_ubyte0_e32 v85, v21
	v_cvt_f32_ubyte1_e32 v86, v21
	v_cvt_f32_ubyte2_e32 v87, v21
	v_cvt_f32_ubyte3_e32 v88, v21
	v_fmac_f32_e32 v6, v85, v52
	v_fmac_f32_e32 v7, v86, v52
	v_fmac_f32_e32 v8, v87, v52
	v_fmac_f32_e32 v9, v88, v52
	v_cvt_f32_ubyte0_e32 v85, v22
	v_cvt_f32_ubyte1_e32 v86, v22
	v_cvt_f32_ubyte2_e32 v87, v22
	v_cvt_f32_ubyte3_e32 v88, v22
	v_fmac_f32_e32 v10, v85, v52
	v_fmac_f32_e32 v11, v86, v52
	v_fmac_f32_e32 v12, v87, v52
	v_fmac_f32_e32 v13, v88, v52
	v_cvt_f32_ubyte0_e32 v85, v23
	v_cvt_f32_ubyte1_e32 v86, v23
	v_cvt_f32_ubyte2_e32 v87, v23
	v_cvt_f32_ubyte3_e32 v88, v23
	v_fmac_f32_e32 v14, v85, v52
	v_fmac_f32_e32 v15, v86, v52
	v_fmac_f32_e32 v16, v87, v52
	v_fmac_f32_e32 v17, v88, v52
	v_add_f32_e32 v18, v18, v52
	v_and_b32_e32 v84, 0xffff, v79
	v_lshl_or_b32 v83, v84, 7, v89
	v_cmp_lt_i32_e32 vcc, 24, v78
	s_mov_b64 exec, vcc
	global_load_dwordx4 v[20:23], v83, s[12:13]
	s_mov_b64 exec, -1
	v_lshlrev_b32_e32 v109, 1, v84
	global_load_ushort v52, v109, s[14:15]
	s_waitcnt vmcnt(6)
	v_cvt_f32_f16_e32 v53, v53
	v_cvt_f32_ubyte0_e32 v85, v24
	v_cvt_f32_ubyte1_e32 v86, v24
	v_cvt_f32_ubyte2_e32 v87, v24
	v_cvt_f32_ubyte3_e32 v88, v24
	v_fmac_f32_e32 v2, v85, v53
	v_fmac_f32_e32 v3, v86, v53
	v_fmac_f32_e32 v4, v87, v53
	v_fmac_f32_e32 v5, v88, v53
	v_cvt_f32_ubyte0_e32 v85, v25
	v_cvt_f32_ubyte1_e32 v86, v25
	v_cvt_f32_ubyte2_e32 v87, v25
	v_cvt_f32_ubyte3_e32 v88, v25
	v_fmac_f32_e32 v6, v85, v53
	v_fmac_f32_e32 v7, v86, v53
	v_fmac_f32_e32 v8, v87, v53
	v_fmac_f32_e32 v9, v88, v53
	v_cvt_f32_ubyte0_e32 v85, v26
	v_cvt_f32_ubyte1_e32 v86, v26
	v_cvt_f32_ubyte2_e32 v87, v26
	v_cvt_f32_ubyte3_e32 v88, v26
	v_fmac_f32_e32 v10, v85, v53
	v_fmac_f32_e32 v11, v86, v53
	v_fmac_f32_e32 v12, v87, v53
	v_fmac_f32_e32 v13, v88, v53
	v_cvt_f32_ubyte0_e32 v85, v27
	v_cvt_f32_ubyte1_e32 v86, v27
	v_cvt_f32_ubyte2_e32 v87, v27
	v_cvt_f32_ubyte3_e32 v88, v27
	v_fmac_f32_e32 v14, v85, v53
	v_fmac_f32_e32 v15, v86, v53
	v_fmac_f32_e32 v16, v87, v53
	v_fmac_f32_e32 v17, v88, v53
	v_add_f32_e32 v18, v18, v53
	v_lshrrev_b32_e32 v84, 16, v79
	v_lshl_or_b32 v83, v84, 7, v89
	v_cmp_lt_i32_e32 vcc, 25, v78
	s_mov_b64 exec, vcc
	global_load_dwordx4 v[24:27], v83, s[12:13]
	s_mov_b64 exec, -1
	v_lshlrev_b32_e32 v109, 1, v84
	global_load_ushort v53, v109, s[14:15]
	s_waitcnt lgkmcnt(0)
	ds_bpermute_b32 v79, v90, v74 offset:24
	s_waitcnt vmcnt(6)
	v_cvt_f32_f16_e32 v54, v54
	v_cvt_f32_ubyte0_e32 v85, v28
	v_cvt_f32_ubyte1_e32 v86, v28
	v_cvt_f32_ubyte2_e32 v87, v28
	v_cvt_f32_ubyte3_e32 v88, v28
	v_fmac_f32_e32 v2, v85, v54
	v_fmac_f32_e32 v3, v86, v54
	v_fmac_f32_e32 v4, v87, v54
	v_fmac_f32_e32 v5, v88, v54
	v_cvt_f32_ubyte0_e32 v85, v29
	v_cvt_f32_ubyte1_e32 v86, v29
	v_cvt_f32_ubyte2_e32 v87, v29
	v_cvt_f32_ubyte3_e32 v88, v29
	v_fmac_f32_e32 v6, v85, v54
	v_fmac_f32_e32 v7, v86, v54
	v_fmac_f32_e32 v8, v87, v54
	v_fmac_f32_e32 v9, v88, v54
	v_cvt_f32_ubyte0_e32 v85, v30
	v_cvt_f32_ubyte1_e32 v86, v30
	v_cvt_f32_ubyte2_e32 v87, v30
	v_cvt_f32_ubyte3_e32 v88, v30
	v_fmac_f32_e32 v10, v85, v54
	v_fmac_f32_e32 v11, v86, v54
	v_fmac_f32_e32 v12, v87, v54
	v_fmac_f32_e32 v13, v88, v54
	v_cvt_f32_ubyte0_e32 v85, v31
	v_cvt_f32_ubyte1_e32 v86, v31
	v_cvt_f32_ubyte2_e32 v87, v31
	v_cvt_f32_ubyte3_e32 v88, v31
	v_fmac_f32_e32 v14, v85, v54
	v_fmac_f32_e32 v15, v86, v54
	v_fmac_f32_e32 v16, v87, v54
	v_fmac_f32_e32 v17, v88, v54
	v_add_f32_e32 v18, v18, v54
	v_and_b32_e32 v84, 0xffff, v80
	v_lshl_or_b32 v83, v84, 7, v89
	v_cmp_lt_i32_e32 vcc, 26, v78
	s_mov_b64 exec, vcc
	global_load_dwordx4 v[28:31], v83, s[12:13]
	s_mov_b64 exec, -1
	v_lshlrev_b32_e32 v109, 1, v84
	global_load_ushort v54, v109, s[14:15]
	s_waitcnt vmcnt(6)
	v_cvt_f32_f16_e32 v55, v55
	v_cvt_f32_ubyte0_e32 v85, v32
	v_cvt_f32_ubyte1_e32 v86, v32
	v_cvt_f32_ubyte2_e32 v87, v32
	v_cvt_f32_ubyte3_e32 v88, v32
	v_fmac_f32_e32 v2, v85, v55
	v_fmac_f32_e32 v3, v86, v55
	v_fmac_f32_e32 v4, v87, v55
	v_fmac_f32_e32 v5, v88, v55
	v_cvt_f32_ubyte0_e32 v85, v33
	v_cvt_f32_ubyte1_e32 v86, v33
	v_cvt_f32_ubyte2_e32 v87, v33
	v_cvt_f32_ubyte3_e32 v88, v33
	v_fmac_f32_e32 v6, v85, v55
	v_fmac_f32_e32 v7, v86, v55
	v_fmac_f32_e32 v8, v87, v55
	v_fmac_f32_e32 v9, v88, v55
	v_cvt_f32_ubyte0_e32 v85, v34
	v_cvt_f32_ubyte1_e32 v86, v34
	v_cvt_f32_ubyte2_e32 v87, v34
	v_cvt_f32_ubyte3_e32 v88, v34
	v_fmac_f32_e32 v10, v85, v55
	v_fmac_f32_e32 v11, v86, v55
	v_fmac_f32_e32 v12, v87, v55
	v_fmac_f32_e32 v13, v88, v55
	v_cvt_f32_ubyte0_e32 v85, v35
	v_cvt_f32_ubyte1_e32 v86, v35
	v_cvt_f32_ubyte2_e32 v87, v35
	v_cvt_f32_ubyte3_e32 v88, v35
	v_fmac_f32_e32 v14, v85, v55
	v_fmac_f32_e32 v15, v86, v55
	v_fmac_f32_e32 v16, v87, v55
	v_fmac_f32_e32 v17, v88, v55
	v_add_f32_e32 v18, v18, v55
	v_lshrrev_b32_e32 v84, 16, v80
	v_lshl_or_b32 v83, v84, 7, v89
	v_cmp_lt_i32_e32 vcc, 27, v78
	s_mov_b64 exec, vcc
	global_load_dwordx4 v[32:35], v83, s[12:13]
	s_mov_b64 exec, -1
	v_lshlrev_b32_e32 v109, 1, v84
	global_load_ushort v55, v109, s[14:15]
	s_cmp_le_u32 s40, 28
	s_cbranch_scc1 .Lg1_tail0
	s_waitcnt lgkmcnt(0)
	ds_bpermute_b32 v80, v90, v74 offset:28
	s_waitcnt vmcnt(6)
	v_cvt_f32_f16_e32 v52, v52
	v_cvt_f32_ubyte0_e32 v85, v20
	v_cvt_f32_ubyte1_e32 v86, v20
	v_cvt_f32_ubyte2_e32 v87, v20
	v_cvt_f32_ubyte3_e32 v88, v20
	v_fmac_f32_e32 v2, v85, v52
	v_fmac_f32_e32 v3, v86, v52
	v_fmac_f32_e32 v4, v87, v52
	v_fmac_f32_e32 v5, v88, v52
	v_cvt_f32_ubyte0_e32 v85, v21
	v_cvt_f32_ubyte1_e32 v86, v21
	v_cvt_f32_ubyte2_e32 v87, v21
	v_cvt_f32_ubyte3_e32 v88, v21
	v_fmac_f32_e32 v6, v85, v52
	v_fmac_f32_e32 v7, v86, v52
	v_fmac_f32_e32 v8, v87, v52
	v_fmac_f32_e32 v9, v88, v52
	v_cvt_f32_ubyte0_e32 v85, v22
	v_cvt_f32_ubyte1_e32 v86, v22
	v_cvt_f32_ubyte2_e32 v87, v22
	v_cvt_f32_ubyte3_e32 v88, v22
	v_fmac_f32_e32 v10, v85, v52
	v_fmac_f32_e32 v11, v86, v52
	v_fmac_f32_e32 v12, v87, v52
	v_fmac_f32_e32 v13, v88, v52
	v_cvt_f32_ubyte0_e32 v85, v23
	v_cvt_f32_ubyte1_e32 v86, v23
	v_cvt_f32_ubyte2_e32 v87, v23
	v_cvt_f32_ubyte3_e32 v88, v23
	v_fmac_f32_e32 v14, v85, v52
	v_fmac_f32_e32 v15, v86, v52
	v_fmac_f32_e32 v16, v87, v52
	v_fmac_f32_e32 v17, v88, v52
	v_add_f32_e32 v18, v18, v52
	v_and_b32_e32 v84, 0xffff, v79
	v_lshl_or_b32 v83, v84, 7, v89
	v_cmp_lt_i32_e32 vcc, 28, v78
	s_mov_b64 exec, vcc
	global_load_dwordx4 v[20:23], v83, s[12:13]
	s_mov_b64 exec, -1
	v_lshlrev_b32_e32 v109, 1, v84
	global_load_ushort v52, v109, s[14:15]
	s_waitcnt vmcnt(6)
	v_cvt_f32_f16_e32 v53, v53
	v_cvt_f32_ubyte0_e32 v85, v24
	v_cvt_f32_ubyte1_e32 v86, v24
	v_cvt_f32_ubyte2_e32 v87, v24
	v_cvt_f32_ubyte3_e32 v88, v24
	v_fmac_f32_e32 v2, v85, v53
	v_fmac_f32_e32 v3, v86, v53
	v_fmac_f32_e32 v4, v87, v53
	v_fmac_f32_e32 v5, v88, v53
	v_cvt_f32_ubyte0_e32 v85, v25
	v_cvt_f32_ubyte1_e32 v86, v25
	v_cvt_f32_ubyte2_e32 v87, v25
	v_cvt_f32_ubyte3_e32 v88, v25
	v_fmac_f32_e32 v6, v85, v53
	v_fmac_f32_e32 v7, v86, v53
	v_fmac_f32_e32 v8, v87, v53
	v_fmac_f32_e32 v9, v88, v53
	v_cvt_f32_ubyte0_e32 v85, v26
	v_cvt_f32_ubyte1_e32 v86, v26
	v_cvt_f32_ubyte2_e32 v87, v26
	v_cvt_f32_ubyte3_e32 v88, v26
	v_fmac_f32_e32 v10, v85, v53
	v_fmac_f32_e32 v11, v86, v53
	v_fmac_f32_e32 v12, v87, v53
	v_fmac_f32_e32 v13, v88, v53
	v_cvt_f32_ubyte0_e32 v85, v27
	v_cvt_f32_ubyte1_e32 v86, v27
	v_cvt_f32_ubyte2_e32 v87, v27
	v_cvt_f32_ubyte3_e32 v88, v27
	v_fmac_f32_e32 v14, v85, v53
	v_fmac_f32_e32 v15, v86, v53
	v_fmac_f32_e32 v16, v87, v53
	v_fmac_f32_e32 v17, v88, v53
	v_add_f32_e32 v18, v18, v53
	v_lshrrev_b32_e32 v84, 16, v79
	v_lshl_or_b32 v83, v84, 7, v89
	v_cmp_lt_i32_e32 vcc, 29, v78
	s_mov_b64 exec, vcc
	global_load_dwordx4 v[24:27], v83, s[12:13]
	s_mov_b64 exec, -1
	v_lshlrev_b32_e32 v109, 1, v84
	global_load_ushort v53, v109, s[14:15]
	s_waitcnt lgkmcnt(0)
	s_waitcnt vmcnt(6)
	v_cvt_f32_f16_e32 v54, v54
	v_cvt_f32_ubyte0_e32 v85, v28
	v_cvt_f32_ubyte1_e32 v86, v28
	v_cvt_f32_ubyte2_e32 v87, v28
	v_cvt_f32_ubyte3_e32 v88, v28
	v_fmac_f32_e32 v2, v85, v54
	v_fmac_f32_e32 v3, v86, v54
	v_fmac_f32_e32 v4, v87, v54
	v_fmac_f32_e32 v5, v88, v54
	v_cvt_f32_ubyte0_e32 v85, v29
	v_cvt_f32_ubyte1_e32 v86, v29
	v_cvt_f32_ubyte2_e32 v87, v29
	v_cvt_f32_ubyte3_e32 v88, v29
	v_fmac_f32_e32 v6, v85, v54
	v_fmac_f32_e32 v7, v86, v54
	v_fmac_f32_e32 v8, v87, v54
	v_fmac_f32_e32 v9, v88, v54
	v_cvt_f32_ubyte0_e32 v85, v30
	v_cvt_f32_ubyte1_e32 v86, v30
	v_cvt_f32_ubyte2_e32 v87, v30
	v_cvt_f32_ubyte3_e32 v88, v30
	v_fmac_f32_e32 v10, v85, v54
	v_fmac_f32_e32 v11, v86, v54
	v_fmac_f32_e32 v12, v87, v54
	v_fmac_f32_e32 v13, v88, v54
	v_cvt_f32_ubyte0_e32 v85, v31
	v_cvt_f32_ubyte1_e32 v86, v31
	v_cvt_f32_ubyte2_e32 v87, v31
	v_cvt_f32_ubyte3_e32 v88, v31
	v_fmac_f32_e32 v14, v85, v54
	v_fmac_f32_e32 v15, v86, v54
	v_fmac_f32_e32 v16, v87, v54
	v_fmac_f32_e32 v17, v88, v54
	v_add_f32_e32 v18, v18, v54
	v_and_b32_e32 v84, 0xffff, v80
	v_lshl_or_b32 v83, v84, 7, v89
	v_cmp_lt_i32_e32 vcc, 30, v78
	s_mov_b64 exec, vcc
	global_load_dwordx4 v[28:31], v83, s[12:13]
	s_mov_b64 exec, -1
	v_lshlrev_b32_e32 v109, 1, v84
	global_load_ushort v54, v109, s[14:15]
	s_waitcnt vmcnt(6)
	v_cvt_f32_f16_e32 v55, v55
	v_cvt_f32_ubyte0_e32 v85, v32
	v_cvt_f32_ubyte1_e32 v86, v32
	v_cvt_f32_ubyte2_e32 v87, v32
	v_cvt_f32_ubyte3_e32 v88, v32
	v_fmac_f32_e32 v2, v85, v55
	v_fmac_f32_e32 v3, v86, v55
	v_fmac_f32_e32 v4, v87, v55
	v_fmac_f32_e32 v5, v88, v55
	v_cvt_f32_ubyte0_e32 v85, v33
	v_cvt_f32_ubyte1_e32 v86, v33
	v_cvt_f32_ubyte2_e32 v87, v33
	v_cvt_f32_ubyte3_e32 v88, v33
	v_fmac_f32_e32 v6, v85, v55
	v_fmac_f32_e32 v7, v86, v55
	v_fmac_f32_e32 v8, v87, v55
	v_fmac_f32_e32 v9, v88, v55
	v_cvt_f32_ubyte0_e32 v85, v34
	v_cvt_f32_ubyte1_e32 v86, v34
	v_cvt_f32_ubyte2_e32 v87, v34
	v_cvt_f32_ubyte3_e32 v88, v34
	v_fmac_f32_e32 v10, v85, v55
	v_fmac_f32_e32 v11, v86, v55
	v_fmac_f32_e32 v12, v87, v55
	v_fmac_f32_e32 v13, v88, v55
	v_cvt_f32_ubyte0_e32 v85, v35
	v_cvt_f32_ubyte1_e32 v86, v35
	v_cvt_f32_ubyte2_e32 v87, v35
	v_cvt_f32_ubyte3_e32 v88, v35
	v_fmac_f32_e32 v14, v85, v55
	v_fmac_f32_e32 v15, v86, v55
	v_fmac_f32_e32 v16, v87, v55
	v_fmac_f32_e32 v17, v88, v55
	v_add_f32_e32 v18, v18, v55
	v_lshrrev_b32_e32 v84, 16, v80
	v_lshl_or_b32 v83, v84, 7, v89
	v_cmp_lt_i32_e32 vcc, 31, v78
	s_mov_b64 exec, vcc
	global_load_dwordx4 v[32:35], v83, s[12:13]
	s_mov_b64 exec, -1
	v_lshlrev_b32_e32 v109, 1, v84
	global_load_ushort v55, v109, s[14:15]
.Lg1_tail0:
	s_cmp_eq_u32 s39, 1
	s_cbranch_scc1 .Lg1_tailb0
	s_waitcnt vmcnt(6)
	v_cvt_f32_f16_e32 v52, v52
	v_cvt_f32_ubyte0_e32 v85, v20
	v_cvt_f32_ubyte1_e32 v86, v20
	v_cvt_f32_ubyte2_e32 v87, v20
	v_cvt_f32_ubyte3_e32 v88, v20
	v_fmac_f32_e32 v2, v85, v52
	v_fmac_f32_e32 v3, v86, v52
	v_fmac_f32_e32 v4, v87, v52
	v_fmac_f32_e32 v5, v88, v52
	v_cvt_f32_ubyte0_e32 v85, v21
	v_cvt_f32_ubyte1_e32 v86, v21
	v_cvt_f32_ubyte2_e32 v87, v21
	v_cvt_f32_ubyte3_e32 v88, v21
	v_fmac_f32_e32 v6, v85, v52
	v_fmac_f32_e32 v7, v86, v52
	v_fmac_f32_e32 v8, v87, v52
	v_fmac_f32_e32 v9, v88, v52
	v_cvt_f32_ubyte0_e32 v85, v22
	v_cvt_f32_ubyte1_e32 v86, v22
	v_cvt_f32_ubyte2_e32 v87, v22
	v_cvt_f32_ubyte3_e32 v88, v22
	v_fmac_f32_e32 v10, v85, v52
	v_fmac_f32_e32 v11, v86, v52
	v_fmac_f32_e32 v12, v87, v52
	v_fmac_f32_e32 v13, v88, v52
	v_cvt_f32_ubyte0_e32 v85, v23
	v_cvt_f32_ubyte1_e32 v86, v23
	v_cvt_f32_ubyte2_e32 v87, v23
	v_cvt_f32_ubyte3_e32 v88, v23
	v_fmac_f32_e32 v14, v85, v52
	v_fmac_f32_e32 v15, v86, v52
	v_fmac_f32_e32 v16, v87, v52
	v_fmac_f32_e32 v17, v88, v52
	v_add_f32_e32 v18, v18, v52
	s_waitcnt vmcnt(4)
	v_cvt_f32_f16_e32 v53, v53
	v_cvt_f32_ubyte0_e32 v85, v24
	v_cvt_f32_ubyte1_e32 v86, v24
	v_cvt_f32_ubyte2_e32 v87, v24
	v_cvt_f32_ubyte3_e32 v88, v24
	v_fmac_f32_e32 v2, v85, v53
	v_fmac_f32_e32 v3, v86, v53
	v_fmac_f32_e32 v4, v87, v53
	v_fmac_f32_e32 v5, v88, v53
	v_cvt_f32_ubyte0_e32 v85, v25
	v_cvt_f32_ubyte1_e32 v86, v25
	v_cvt_f32_ubyte2_e32 v87, v25
	v_cvt_f32_ubyte3_e32 v88, v25
	v_fmac_f32_e32 v6, v85, v53
	v_fmac_f32_e32 v7, v86, v53
	v_fmac_f32_e32 v8, v87, v53
	v_fmac_f32_e32 v9, v88, v53
	v_cvt_f32_ubyte0_e32 v85, v26
	v_cvt_f32_ubyte1_e32 v86, v26
	v_cvt_f32_ubyte2_e32 v87, v26
	v_cvt_f32_ubyte3_e32 v88, v26
	v_fmac_f32_e32 v10, v85, v53
	v_fmac_f32_e32 v11, v86, v53
	v_fmac_f32_e32 v12, v87, v53
	v_fmac_f32_e32 v13, v88, v53
	v_cvt_f32_ubyte0_e32 v85, v27
	v_cvt_f32_ubyte1_e32 v86, v27
	v_cvt_f32_ubyte2_e32 v87, v27
	v_cvt_f32_ubyte3_e32 v88, v27
	v_fmac_f32_e32 v14, v85, v53
	v_fmac_f32_e32 v15, v86, v53
	v_fmac_f32_e32 v16, v87, v53
	v_fmac_f32_e32 v17, v88, v53
	v_add_f32_e32 v18, v18, v53
	s_waitcnt vmcnt(2)
	v_cvt_f32_f16_e32 v54, v54
	v_cvt_f32_ubyte0_e32 v85, v28
	v_cvt_f32_ubyte1_e32 v86, v28
	v_cvt_f32_ubyte2_e32 v87, v28
	v_cvt_f32_ubyte3_e32 v88, v28
	v_fmac_f32_e32 v2, v85, v54
	v_fmac_f32_e32 v3, v86, v54
	v_fmac_f32_e32 v4, v87, v54
	v_fmac_f32_e32 v5, v88, v54
	v_cvt_f32_ubyte0_e32 v85, v29
	v_cvt_f32_ubyte1_e32 v86, v29
	v_cvt_f32_ubyte2_e32 v87, v29
	v_cvt_f32_ubyte3_e32 v88, v29
	v_fmac_f32_e32 v6, v85, v54
	v_fmac_f32_e32 v7, v86, v54
	v_fmac_f32_e32 v8, v87, v54
	v_fmac_f32_e32 v9, v88, v54
	v_cvt_f32_ubyte0_e32 v85, v30
	v_cvt_f32_ubyte1_e32 v86, v30
	v_cvt_f32_ubyte2_e32 v87, v30
	v_cvt_f32_ubyte3_e32 v88, v30
	v_fmac_f32_e32 v10, v85, v54
	v_fmac_f32_e32 v11, v86, v54
	v_fmac_f32_e32 v12, v87, v54
	v_fmac_f32_e32 v13, v88, v54
	v_cvt_f32_ubyte0_e32 v85, v31
	v_cvt_f32_ubyte1_e32 v86, v31
	v_cvt_f32_ubyte2_e32 v87, v31
	v_cvt_f32_ubyte3_e32 v88, v31
	v_fmac_f32_e32 v14, v85, v54
	v_fmac_f32_e32 v15, v86, v54
	v_fmac_f32_e32 v16, v87, v54
	v_fmac_f32_e32 v17, v88, v54
	v_add_f32_e32 v18, v18, v54
	s_waitcnt vmcnt(0)
	v_cvt_f32_f16_e32 v55, v55
	v_cvt_f32_ubyte0_e32 v85, v32
	v_cvt_f32_ubyte1_e32 v86, v32
	v_cvt_f32_ubyte2_e32 v87, v32
	v_cvt_f32_ubyte3_e32 v88, v32
	v_fmac_f32_e32 v2, v85, v55
	v_fmac_f32_e32 v3, v86, v55
	v_fmac_f32_e32 v4, v87, v55
	v_fmac_f32_e32 v5, v88, v55
	v_cvt_f32_ubyte0_e32 v85, v33
	v_cvt_f32_ubyte1_e32 v86, v33
	v_cvt_f32_ubyte2_e32 v87, v33
	v_cvt_f32_ubyte3_e32 v88, v33
	v_fmac_f32_e32 v6, v85, v55
	v_fmac_f32_e32 v7, v86, v55
	v_fmac_f32_e32 v8, v87, v55
	v_fmac_f32_e32 v9, v88, v55
	v_cvt_f32_ubyte0_e32 v85, v34
	v_cvt_f32_ubyte1_e32 v86, v34
	v_cvt_f32_ubyte2_e32 v87, v34
	v_cvt_f32_ubyte3_e32 v88, v34
	v_fmac_f32_e32 v10, v85, v55
	v_fmac_f32_e32 v11, v86, v55
	v_fmac_f32_e32 v12, v87, v55
	v_fmac_f32_e32 v13, v88, v55
	v_cvt_f32_ubyte0_e32 v85, v35
	v_cvt_f32_ubyte1_e32 v86, v35
	v_cvt_f32_ubyte2_e32 v87, v35
	v_cvt_f32_ubyte3_e32 v88, v35
	v_fmac_f32_e32 v14, v85, v55
	v_fmac_f32_e32 v15, v86, v55
	v_fmac_f32_e32 v16, v87, v55
	v_fmac_f32_e32 v17, v88, v55
	v_add_f32_e32 v18, v18, v55
	s_branch .Lg1_rare_check
.Lg1_tailb0:
	global_load_dwordx4 v[36:39], v103, s[8:9] offset:256
	global_load_dwordx4 v[40:43], v103, s[8:9] offset:272
	global_load_dwordx4 v[44:47], v103, s[8:9] offset:384
	global_load_dwordx4 v[48:51], v103, s[8:9] offset:400
	s_waitcnt vmcnt(10)
	v_cvt_f32_f16_e32 v52, v52
	v_cvt_f32_ubyte0_e32 v85, v20
	v_cvt_f32_ubyte1_e32 v86, v20
	v_cvt_f32_ubyte2_e32 v87, v20
	v_cvt_f32_ubyte3_e32 v88, v20
	v_fmac_f32_e32 v2, v85, v52
	v_fmac_f32_e32 v3, v86, v52
	v_fmac_f32_e32 v4, v87, v52
	v_fmac_f32_e32 v5, v88, v52
	v_cvt_f32_ubyte0_e32 v85, v21
	v_cvt_f32_ubyte1_e32 v86, v21
	v_cvt_f32_ubyte2_e32 v87, v21
	v_cvt_f32_ubyte3_e32 v88, v21
	v_fmac_f32_e32 v6, v85, v52
	v_fmac_f32_e32 v7, v86, v52
	v_fmac_f32_e32 v8, v87, v52
	v_fmac_f32_e32 v9, v88, v52
	v_cvt_f32_ubyte0_e32 v85, v22
	v_cvt_f32_ubyte1_e32 v86, v22
	v_cvt_f32_ubyte2_e32 v87, v22
	v_cvt_f32_ubyte3_e32 v88, v22
	v_fmac_f32_e32 v10, v85, v52
	v_fmac_f32_e32 v11, v86, v52
	v_fmac_f32_e32 v12, v87, v52
	v_fmac_f32_e32 v13, v88, v52
	v_cvt_f32_ubyte0_e32 v85, v23
	v_cvt_f32_ubyte1_e32 v86, v23
	v_cvt_f32_ubyte2_e32 v87, v23
	v_cvt_f32_ubyte3_e32 v88, v23
	v_fmac_f32_e32 v14, v85, v52
	v_fmac_f32_e32 v15, v86, v52
	v_fmac_f32_e32 v16, v87, v52
	v_fmac_f32_e32 v17, v88, v52
	v_add_f32_e32 v18, v18, v52
	global_load_dwordx4 v[20:23], v103, s[8:9] offset:0
	s_waitcnt vmcnt(9)
	v_cvt_f32_f16_e32 v53, v53
	v_cvt_f32_ubyte0_e32 v85, v24
	v_cvt_f32_ubyte1_e32 v86, v24
	v_cvt_f32_ubyte2_e32 v87, v24
	v_cvt_f32_ubyte3_e32 v88, v24
	v_fmac_f32_e32 v2, v85, v53
	v_fmac_f32_e32 v3, v86, v53
	v_fmac_f32_e32 v4, v87, v53
	v_fmac_f32_e32 v5, v88, v53
	v_cvt_f32_ubyte0_e32 v85, v25
	v_cvt_f32_ubyte1_e32 v86, v25
	v_cvt_f32_ubyte2_e32 v87, v25
	v_cvt_f32_ubyte3_e32 v88, v25
	v_fmac_f32_e32 v6, v85, v53
	v_fmac_f32_e32 v7, v86, v53
	v_fmac_f32_e32 v8, v87, v53
	v_fmac_f32_e32 v9, v88, v53
	v_cvt_f32_ubyte0_e32 v85, v26
	v_cvt_f32_ubyte1_e32 v86, v26
	v_cvt_f32_ubyte2_e32 v87, v26
	v_cvt_f32_ubyte3_e32 v88, v26
	v_fmac_f32_e32 v10, v85, v53
	v_fmac_f32_e32 v11, v86, v53
	v_fmac_f32_e32 v12, v87, v53
	v_fmac_f32_e32 v13, v88, v53
	v_cvt_f32_ubyte0_e32 v85, v27
	v_cvt_f32_ubyte1_e32 v86, v27
	v_cvt_f32_ubyte2_e32 v87, v27
	v_cvt_f32_ubyte3_e32 v88, v27
	v_fmac_f32_e32 v14, v85, v53
	v_fmac_f32_e32 v15, v86, v53
	v_fmac_f32_e32 v16, v87, v53
	v_fmac_f32_e32 v17, v88, v53
	v_add_f32_e32 v18, v18, v53
	global_load_dwordx4 v[24:27], v103, s[8:9] offset:16
	s_waitcnt vmcnt(8)
	v_cvt_f32_f16_e32 v54, v54
	v_cvt_f32_ubyte0_e32 v85, v28
	v_cvt_f32_ubyte1_e32 v86, v28
	v_cvt_f32_ubyte2_e32 v87, v28
	v_cvt_f32_ubyte3_e32 v88, v28
	v_fmac_f32_e32 v2, v85, v54
	v_fmac_f32_e32 v3, v86, v54
	v_fmac_f32_e32 v4, v87, v54
	v_fmac_f32_e32 v5, v88, v54
	v_cvt_f32_ubyte0_e32 v85, v29
	v_cvt_f32_ubyte1_e32 v86, v29
	v_cvt_f32_ubyte2_e32 v87, v29
	v_cvt_f32_ubyte3_e32 v88, v29
	v_fmac_f32_e32 v6, v85, v54
	v_fmac_f32_e32 v7, v86, v54
	v_fmac_f32_e32 v8, v87, v54
	v_fmac_f32_e32 v9, v88, v54
	v_cvt_f32_ubyte0_e32 v85, v30
	v_cvt_f32_ubyte1_e32 v86, v30
	v_cvt_f32_ubyte2_e32 v87, v30
	v_cvt_f32_ubyte3_e32 v88, v30
	v_fmac_f32_e32 v10, v85, v54
	v_fmac_f32_e32 v11, v86, v54
	v_fmac_f32_e32 v12, v87, v54
	v_fmac_f32_e32 v13, v88, v54
	v_cvt_f32_ubyte0_e32 v85, v31
	v_cvt_f32_ubyte1_e32 v86, v31
	v_cvt_f32_ubyte2_e32 v87, v31
	v_cvt_f32_ubyte3_e32 v88, v31
	v_fmac_f32_e32 v14, v85, v54
	v_fmac_f32_e32 v15, v86, v54
	v_fmac_f32_e32 v16, v87, v54
	v_fmac_f32_e32 v17, v88, v54
	v_add_f32_e32 v18, v18, v54
	global_load_dwordx4 v[28:31], v103, s[8:9] offset:128
	s_waitcnt vmcnt(7)
	v_cvt_f32_f16_e32 v55, v55
	v_cvt_f32_ubyte0_e32 v85, v32
	v_cvt_f32_ubyte1_e32 v86, v32
	v_cvt_f32_ubyte2_e32 v87, v32
	v_cvt_f32_ubyte3_e32 v88, v32
	v_fmac_f32_e32 v2, v85, v55
	v_fmac_f32_e32 v3, v86, v55
	v_fmac_f32_e32 v4, v87, v55
	v_fmac_f32_e32 v5, v88, v55
	v_cvt_f32_ubyte0_e32 v85, v33
	v_cvt_f32_ubyte1_e32 v86, v33
	v_cvt_f32_ubyte2_e32 v87, v33
	v_cvt_f32_ubyte3_e32 v88, v33
	v_fmac_f32_e32 v6, v85, v55
	v_fmac_f32_e32 v7, v86, v55
	v_fmac_f32_e32 v8, v87, v55
	v_fmac_f32_e32 v9, v88, v55
	v_cvt_f32_ubyte0_e32 v85, v34
	v_cvt_f32_ubyte1_e32 v86, v34
	v_cvt_f32_ubyte2_e32 v87, v34
	v_cvt_f32_ubyte3_e32 v88, v34
	v_fmac_f32_e32 v10, v85, v55
	v_fmac_f32_e32 v11, v86, v55
	v_fmac_f32_e32 v12, v87, v55
	v_fmac_f32_e32 v13, v88, v55
	v_cvt_f32_ubyte0_e32 v85, v35
	v_cvt_f32_ubyte1_e32 v86, v35
	v_cvt_f32_ubyte2_e32 v87, v35
	v_cvt_f32_ubyte3_e32 v88, v35
	v_fmac_f32_e32 v14, v85, v55
	v_fmac_f32_e32 v15, v86, v55
	v_fmac_f32_e32 v16, v87, v55
	v_fmac_f32_e32 v17, v88, v55
	v_add_f32_e32 v18, v18, v55
	global_load_dwordx4 v[32:35], v103, s[8:9] offset:144
	s_branch .Lg1_rare_check
